# speedup vs baseline: 1.0285x; 1.0081x over previous
_Z9k2_colsumPKDv8_DF16_S1_Pf:
	s_load_dwordx4 s[4:7], s[0:1], 0x0
	s_load_dwordx2 s[8:9], s[0:1], 0x10
	v_mov_b32_e32 v170, v0
	v_and_b32_e32 v172, 63, v0
	v_lshrrev_b32_e32 v173, 6, v0
	v_lshlrev_b32_e32 v171, 4, v172
	v_add_u32_e32 v174, 0x1000, v171
	s_lshr_b32 s10, s2, 6
	s_and_b32 s11, s2, 63
	s_lshl_b32 s11, s11, 1
	s_lshl_b32 s12, s10, 7
	s_add_u32 s13, s12, s11
	s_lshl_b32 s13, s13, 12
	v_readfirstlane_b32 s14, v173
	s_nop 3
	s_lshl_b32 s15, s14, 4
	s_add_u32 s15, s15, s12
	s_lshl_b32 s15, s15, 12
	s_waitcnt lgkmcnt(0)
	s_add_u32 s6, s6, s13
	s_addc_u32 s7, s7, 0
	s_add_u32 s4, s4, s15
	s_addc_u32 s5, s5, 0
	global_load_dwordx4 v[0:3], v171, s[6:7] offset:0
	global_load_dwordx4 v[4:7], v171, s[6:7] offset:1024
	global_load_dwordx4 v[8:11], v171, s[6:7] offset:2048
	global_load_dwordx4 v[12:15], v171, s[6:7] offset:3072
	global_load_dwordx4 v[16:19], v174, s[6:7] offset:0
	global_load_dwordx4 v[20:23], v174, s[6:7] offset:1024
	global_load_dwordx4 v[24:27], v174, s[6:7] offset:2048
	global_load_dwordx4 v[28:31], v174, s[6:7] offset:3072
	global_load_dwordx4 v[32:35], v171, s[4:5] offset:0
	global_load_dwordx4 v[36:39], v171, s[4:5] offset:1024
	global_load_dwordx4 v[40:43], v171, s[4:5] offset:2048
	global_load_dwordx4 v[44:47], v171, s[4:5] offset:3072
	s_add_u32 s4, s4, 0x1000
	s_addc_u32 s5, s5, 0
	global_load_dwordx4 v[48:51], v171, s[4:5] offset:0
	global_load_dwordx4 v[52:55], v171, s[4:5] offset:1024
	global_load_dwordx4 v[56:59], v171, s[4:5] offset:2048
	global_load_dwordx4 v[60:63], v171, s[4:5] offset:3072
	s_add_u32 s4, s4, 0x1000
	s_addc_u32 s5, s5, 0
	global_load_dwordx4 v[64:67], v171, s[4:5] offset:0
	global_load_dwordx4 v[68:71], v171, s[4:5] offset:1024
	global_load_dwordx4 v[72:75], v171, s[4:5] offset:2048
	global_load_dwordx4 v[76:79], v171, s[4:5] offset:3072
	s_add_u32 s4, s4, 0x1000
	s_addc_u32 s5, s5, 0
	global_load_dwordx4 v[80:83], v171, s[4:5] offset:0
	global_load_dwordx4 v[84:87], v171, s[4:5] offset:1024
	global_load_dwordx4 v[88:91], v171, s[4:5] offset:2048
	global_load_dwordx4 v[92:95], v171, s[4:5] offset:3072
	s_add_u32 s4, s4, 0x1000
	s_addc_u32 s5, s5, 0
	v_mov_b32_e32 v160, 0
	v_mov_b32_e32 v161, 0
	v_mov_b32_e32 v162, 0
	v_mov_b32_e32 v163, 0
	v_mov_b32_e32 v164, 0
	v_mov_b32_e32 v165, 0
	v_mov_b32_e32 v166, 0
	v_mov_b32_e32 v167, 0
	s_cmp_lt_u32 s14, 4
	s_cbranch_scc1 .Lk2_older
	s_setprio 1
	s_sleep 4
.Lk2_older:
	s_waitcnt vmcnt(12)
	v_mfma_f32_32x32x16_f16 v[96:111], v[32:35], v[0:3], 0
	v_mfma_f32_32x32x16_f16 v[112:127], v[32:35], v[16:19], 0
	v_mfma_f32_32x32x16_f16 v[96:111], v[36:39], v[4:7], v[96:111]
	v_mfma_f32_32x32x16_f16 v[112:127], v[36:39], v[20:23], v[112:127]
	v_mfma_f32_32x32x16_f16 v[96:111], v[40:43], v[8:11], v[96:111]
	v_mfma_f32_32x32x16_f16 v[112:127], v[40:43], v[24:27], v[112:127]
	v_mfma_f32_32x32x16_f16 v[96:111], v[44:47], v[12:15], v[96:111]
	v_mfma_f32_32x32x16_f16 v[112:127], v[44:47], v[28:31], v[112:127]
	global_load_dwordx4 v[32:35], v171, s[4:5] offset:0
	global_load_dwordx4 v[36:39], v171, s[4:5] offset:1024
	global_load_dwordx4 v[40:43], v171, s[4:5] offset:2048
	global_load_dwordx4 v[44:47], v171, s[4:5] offset:3072
	s_add_u32 s4, s4, 0x1000
	s_addc_u32 s5, s5, 0
	s_nop 7
	s_nop 3
	s_waitcnt vmcnt(12)
	v_mfma_f32_32x32x16_f16 v[128:143], v[48:51], v[0:3], 0
	v_exp_f32_e32 v96, v96
	v_exp_f32_e32 v97, v97
	v_exp_f32_e32 v98, v98
	v_exp_f32_e32 v99, v99
	v_mfma_f32_32x32x16_f16 v[144:159], v[48:51], v[16:19], 0
	v_exp_f32_e32 v100, v100
	v_exp_f32_e32 v101, v101
	v_exp_f32_e32 v102, v102
	v_exp_f32_e32 v103, v103
	v_pk_add_f32 v[160:161], v[160:161], v[96:97]
	v_pk_add_f32 v[162:163], v[162:163], v[98:99]
	v_mfma_f32_32x32x16_f16 v[128:143], v[52:55], v[4:7], v[128:143]
	v_exp_f32_e32 v104, v104
	v_exp_f32_e32 v105, v105
	v_exp_f32_e32 v106, v106
	v_exp_f32_e32 v107, v107
	v_pk_add_f32 v[160:161], v[160:161], v[100:101]
	v_pk_add_f32 v[162:163], v[162:163], v[102:103]
	v_mfma_f32_32x32x16_f16 v[144:159], v[52:55], v[20:23], v[144:159]
	v_exp_f32_e32 v108, v108
	v_exp_f32_e32 v109, v109
	v_exp_f32_e32 v110, v110
	v_exp_f32_e32 v111, v111
	v_pk_add_f32 v[160:161], v[160:161], v[104:105]
	v_pk_add_f32 v[162:163], v[162:163], v[106:107]
	v_mfma_f32_32x32x16_f16 v[128:143], v[56:59], v[8:11], v[128:143]
	v_exp_f32_e32 v112, v112
	v_exp_f32_e32 v113, v113
	v_exp_f32_e32 v114, v114
	v_exp_f32_e32 v115, v115
	v_pk_add_f32 v[160:161], v[160:161], v[108:109]
	v_pk_add_f32 v[162:163], v[162:163], v[110:111]
	v_mfma_f32_32x32x16_f16 v[144:159], v[56:59], v[24:27], v[144:159]
	v_exp_f32_e32 v116, v116
	v_exp_f32_e32 v117, v117
	v_exp_f32_e32 v118, v118
	v_exp_f32_e32 v119, v119
	v_pk_add_f32 v[164:165], v[164:165], v[112:113]
	v_pk_add_f32 v[166:167], v[166:167], v[114:115]
	v_mfma_f32_32x32x16_f16 v[128:143], v[60:63], v[12:15], v[128:143]
	v_exp_f32_e32 v120, v120
	v_exp_f32_e32 v121, v121
	v_exp_f32_e32 v122, v122
	v_exp_f32_e32 v123, v123
	v_pk_add_f32 v[164:165], v[164:165], v[116:117]
	v_pk_add_f32 v[166:167], v[166:167], v[118:119]
	v_mfma_f32_32x32x16_f16 v[144:159], v[60:63], v[28:31], v[144:159]
	v_exp_f32_e32 v124, v124
	v_exp_f32_e32 v125, v125
	v_exp_f32_e32 v126, v126
	v_exp_f32_e32 v127, v127
	v_pk_add_f32 v[164:165], v[164:165], v[120:121]
	v_pk_add_f32 v[166:167], v[166:167], v[122:123]
	s_nop 0
	v_pk_add_f32 v[164:165], v[164:165], v[124:125]
	v_pk_add_f32 v[166:167], v[166:167], v[126:127]
	global_load_dwordx4 v[48:51], v171, s[4:5] offset:0
	global_load_dwordx4 v[52:55], v171, s[4:5] offset:1024
	global_load_dwordx4 v[56:59], v171, s[4:5] offset:2048
	global_load_dwordx4 v[60:63], v171, s[4:5] offset:3072
	s_add_u32 s4, s4, 0x1000
	s_addc_u32 s5, s5, 0
	s_waitcnt vmcnt(12)
	v_mfma_f32_32x32x16_f16 v[96:111], v[64:67], v[0:3], 0
	v_exp_f32_e32 v128, v128
	v_exp_f32_e32 v129, v129
	v_exp_f32_e32 v130, v130
	v_exp_f32_e32 v131, v131
	v_mfma_f32_32x32x16_f16 v[112:127], v[64:67], v[16:19], 0
	v_exp_f32_e32 v132, v132
	v_exp_f32_e32 v133, v133
	v_exp_f32_e32 v134, v134
	v_exp_f32_e32 v135, v135
	v_pk_add_f32 v[160:161], v[160:161], v[128:129]
	v_pk_add_f32 v[162:163], v[162:163], v[130:131]
	v_mfma_f32_32x32x16_f16 v[96:111], v[68:71], v[4:7], v[96:111]
	v_exp_f32_e32 v136, v136
	v_exp_f32_e32 v137, v137
	v_exp_f32_e32 v138, v138
	v_exp_f32_e32 v139, v139
	v_pk_add_f32 v[160:161], v[160:161], v[132:133]
	v_pk_add_f32 v[162:163], v[162:163], v[134:135]
	v_mfma_f32_32x32x16_f16 v[112:127], v[68:71], v[20:23], v[112:127]
	v_exp_f32_e32 v140, v140
	v_exp_f32_e32 v141, v141
	v_exp_f32_e32 v142, v142
	v_exp_f32_e32 v143, v143
	v_pk_add_f32 v[160:161], v[160:161], v[136:137]
	v_pk_add_f32 v[162:163], v[162:163], v[138:139]
	v_mfma_f32_32x32x16_f16 v[96:111], v[72:75], v[8:11], v[96:111]
	v_exp_f32_e32 v144, v144
	v_exp_f32_e32 v145, v145
	v_exp_f32_e32 v146, v146
	v_exp_f32_e32 v147, v147
	v_pk_add_f32 v[160:161], v[160:161], v[140:141]
	v_pk_add_f32 v[162:163], v[162:163], v[142:143]
	v_mfma_f32_32x32x16_f16 v[112:127], v[72:75], v[24:27], v[112:127]
	v_exp_f32_e32 v148, v148
	v_exp_f32_e32 v149, v149
	v_exp_f32_e32 v150, v150
	v_exp_f32_e32 v151, v151
	v_pk_add_f32 v[164:165], v[164:165], v[144:145]
	v_pk_add_f32 v[166:167], v[166:167], v[146:147]
	v_mfma_f32_32x32x16_f16 v[96:111], v[76:79], v[12:15], v[96:111]
	v_exp_f32_e32 v152, v152
	v_exp_f32_e32 v153, v153
	v_exp_f32_e32 v154, v154
	v_exp_f32_e32 v155, v155
	v_pk_add_f32 v[164:165], v[164:165], v[148:149]
	v_pk_add_f32 v[166:167], v[166:167], v[150:151]
	v_mfma_f32_32x32x16_f16 v[112:127], v[76:79], v[28:31], v[112:127]
	v_exp_f32_e32 v156, v156
	v_exp_f32_e32 v157, v157
	v_exp_f32_e32 v158, v158
	v_exp_f32_e32 v159, v159
	v_pk_add_f32 v[164:165], v[164:165], v[152:153]
	v_pk_add_f32 v[166:167], v[166:167], v[154:155]
	s_nop 0
	v_pk_add_f32 v[164:165], v[164:165], v[156:157]
	v_pk_add_f32 v[166:167], v[166:167], v[158:159]
	global_load_dwordx4 v[64:67], v171, s[4:5] offset:0
	global_load_dwordx4 v[68:71], v171, s[4:5] offset:1024
	global_load_dwordx4 v[72:75], v171, s[4:5] offset:2048
	global_load_dwordx4 v[76:79], v171, s[4:5] offset:3072
	s_add_u32 s4, s4, 0x1000
	s_addc_u32 s5, s5, 0
	s_waitcnt vmcnt(12)
	v_mfma_f32_32x32x16_f16 v[128:143], v[80:83], v[0:3], 0
	v_exp_f32_e32 v96, v96
	v_exp_f32_e32 v97, v97
	v_exp_f32_e32 v98, v98
	v_exp_f32_e32 v99, v99
	v_mfma_f32_32x32x16_f16 v[144:159], v[80:83], v[16:19], 0
	v_exp_f32_e32 v100, v100
	v_exp_f32_e32 v101, v101
	v_exp_f32_e32 v102, v102
	v_exp_f32_e32 v103, v103
	v_pk_add_f32 v[160:161], v[160:161], v[96:97]
	v_pk_add_f32 v[162:163], v[162:163], v[98:99]
	v_mfma_f32_32x32x16_f16 v[128:143], v[84:87], v[4:7], v[128:143]
	v_exp_f32_e32 v104, v104
	v_exp_f32_e32 v105, v105
	v_exp_f32_e32 v106, v106
	v_exp_f32_e32 v107, v107
	v_pk_add_f32 v[160:161], v[160:161], v[100:101]
	v_pk_add_f32 v[162:163], v[162:163], v[102:103]
	v_mfma_f32_32x32x16_f16 v[144:159], v[84:87], v[20:23], v[144:159]
	v_exp_f32_e32 v108, v108
	v_exp_f32_e32 v109, v109
	v_exp_f32_e32 v110, v110
	v_exp_f32_e32 v111, v111
	v_pk_add_f32 v[160:161], v[160:161], v[104:105]
	v_pk_add_f32 v[162:163], v[162:163], v[106:107]
	v_mfma_f32_32x32x16_f16 v[128:143], v[88:91], v[8:11], v[128:143]
	v_exp_f32_e32 v112, v112
	v_exp_f32_e32 v113, v113
	v_exp_f32_e32 v114, v114
	v_exp_f32_e32 v115, v115
	v_pk_add_f32 v[160:161], v[160:161], v[108:109]
	v_pk_add_f32 v[162:163], v[162:163], v[110:111]
	v_mfma_f32_32x32x16_f16 v[144:159], v[88:91], v[24:27], v[144:159]
	v_exp_f32_e32 v116, v116
	v_exp_f32_e32 v117, v117
	v_exp_f32_e32 v118, v118
	v_exp_f32_e32 v119, v119
	v_pk_add_f32 v[164:165], v[164:165], v[112:113]
	v_pk_add_f32 v[166:167], v[166:167], v[114:115]
	v_mfma_f32_32x32x16_f16 v[128:143], v[92:95], v[12:15], v[128:143]
	v_exp_f32_e32 v120, v120
	v_exp_f32_e32 v121, v121
	v_exp_f32_e32 v122, v122
	v_exp_f32_e32 v123, v123
	v_pk_add_f32 v[164:165], v[164:165], v[116:117]
	v_pk_add_f32 v[166:167], v[166:167], v[118:119]
	v_mfma_f32_32x32x16_f16 v[144:159], v[92:95], v[28:31], v[144:159]
	v_exp_f32_e32 v124, v124
	v_exp_f32_e32 v125, v125
	v_exp_f32_e32 v126, v126
	v_exp_f32_e32 v127, v127
	v_pk_add_f32 v[164:165], v[164:165], v[120:121]
	v_pk_add_f32 v[166:167], v[166:167], v[122:123]
	s_nop 0
	v_pk_add_f32 v[164:165], v[164:165], v[124:125]
	v_pk_add_f32 v[166:167], v[166:167], v[126:127]
	global_load_dwordx4 v[80:83], v171, s[4:5] offset:0
	global_load_dwordx4 v[84:87], v171, s[4:5] offset:1024
	global_load_dwordx4 v[88:91], v171, s[4:5] offset:2048
	global_load_dwordx4 v[92:95], v171, s[4:5] offset:3072
	s_add_u32 s4, s4, 0x1000
	s_addc_u32 s5, s5, 0
	s_waitcnt vmcnt(12)
	v_mfma_f32_32x32x16_f16 v[96:111], v[32:35], v[0:3], 0
	v_exp_f32_e32 v128, v128
	v_exp_f32_e32 v129, v129
	v_exp_f32_e32 v130, v130
	v_exp_f32_e32 v131, v131
	v_mfma_f32_32x32x16_f16 v[112:127], v[32:35], v[16:19], 0
	v_exp_f32_e32 v132, v132
	v_exp_f32_e32 v133, v133
	v_exp_f32_e32 v134, v134
	v_exp_f32_e32 v135, v135
	v_pk_add_f32 v[160:161], v[160:161], v[128:129]
	v_pk_add_f32 v[162:163], v[162:163], v[130:131]
	v_mfma_f32_32x32x16_f16 v[96:111], v[36:39], v[4:7], v[96:111]
	v_exp_f32_e32 v136, v136
	v_exp_f32_e32 v137, v137
	v_exp_f32_e32 v138, v138
	v_exp_f32_e32 v139, v139
	v_pk_add_f32 v[160:161], v[160:161], v[132:133]
	v_pk_add_f32 v[162:163], v[162:163], v[134:135]
	v_mfma_f32_32x32x16_f16 v[112:127], v[36:39], v[20:23], v[112:127]
	v_exp_f32_e32 v140, v140
	v_exp_f32_e32 v141, v141
	v_exp_f32_e32 v142, v142
	v_exp_f32_e32 v143, v143
	v_pk_add_f32 v[160:161], v[160:161], v[136:137]
	v_pk_add_f32 v[162:163], v[162:163], v[138:139]
	v_mfma_f32_32x32x16_f16 v[96:111], v[40:43], v[8:11], v[96:111]
	v_exp_f32_e32 v144, v144
	v_exp_f32_e32 v145, v145
	v_exp_f32_e32 v146, v146
	v_exp_f32_e32 v147, v147
	v_pk_add_f32 v[160:161], v[160:161], v[140:141]
	v_pk_add_f32 v[162:163], v[162:163], v[142:143]
	v_mfma_f32_32x32x16_f16 v[112:127], v[40:43], v[24:27], v[112:127]
	v_exp_f32_e32 v148, v148
	v_exp_f32_e32 v149, v149
	v_exp_f32_e32 v150, v150
	v_exp_f32_e32 v151, v151
	v_pk_add_f32 v[164:165], v[164:165], v[144:145]
	v_pk_add_f32 v[166:167], v[166:167], v[146:147]
	v_mfma_f32_32x32x16_f16 v[96:111], v[44:47], v[12:15], v[96:111]
	v_exp_f32_e32 v152, v152
	v_exp_f32_e32 v153, v153
	v_exp_f32_e32 v154, v154
	v_exp_f32_e32 v155, v155
	v_pk_add_f32 v[164:165], v[164:165], v[148:149]
	v_pk_add_f32 v[166:167], v[166:167], v[150:151]
	v_mfma_f32_32x32x16_f16 v[112:127], v[44:47], v[28:31], v[112:127]
	v_exp_f32_e32 v156, v156
	v_exp_f32_e32 v157, v157
	v_exp_f32_e32 v158, v158
	v_exp_f32_e32 v159, v159
	v_pk_add_f32 v[164:165], v[164:165], v[152:153]
	v_pk_add_f32 v[166:167], v[166:167], v[154:155]
	s_nop 0
	v_pk_add_f32 v[164:165], v[164:165], v[156:157]
	v_pk_add_f32 v[166:167], v[166:167], v[158:159]
	global_load_dwordx4 v[32:35], v171, s[4:5] offset:0
	global_load_dwordx4 v[36:39], v171, s[4:5] offset:1024
	global_load_dwordx4 v[40:43], v171, s[4:5] offset:2048
	global_load_dwordx4 v[44:47], v171, s[4:5] offset:3072
	s_add_u32 s4, s4, 0x1000
	s_addc_u32 s5, s5, 0
	s_waitcnt vmcnt(12)
	v_mfma_f32_32x32x16_f16 v[128:143], v[48:51], v[0:3], 0
	v_exp_f32_e32 v96, v96
	v_exp_f32_e32 v97, v97
	v_exp_f32_e32 v98, v98
	v_exp_f32_e32 v99, v99
	v_mfma_f32_32x32x16_f16 v[144:159], v[48:51], v[16:19], 0
	v_exp_f32_e32 v100, v100
	v_exp_f32_e32 v101, v101
	v_exp_f32_e32 v102, v102
	v_exp_f32_e32 v103, v103
	v_pk_add_f32 v[160:161], v[160:161], v[96:97]
	v_pk_add_f32 v[162:163], v[162:163], v[98:99]
	v_mfma_f32_32x32x16_f16 v[128:143], v[52:55], v[4:7], v[128:143]
	v_exp_f32_e32 v104, v104
	v_exp_f32_e32 v105, v105
	v_exp_f32_e32 v106, v106
	v_exp_f32_e32 v107, v107
	v_pk_add_f32 v[160:161], v[160:161], v[100:101]
	v_pk_add_f32 v[162:163], v[162:163], v[102:103]
	v_mfma_f32_32x32x16_f16 v[144:159], v[52:55], v[20:23], v[144:159]
	v_exp_f32_e32 v108, v108
	v_exp_f32_e32 v109, v109
	v_exp_f32_e32 v110, v110
	v_exp_f32_e32 v111, v111
	v_pk_add_f32 v[160:161], v[160:161], v[104:105]
	v_pk_add_f32 v[162:163], v[162:163], v[106:107]
	v_mfma_f32_32x32x16_f16 v[128:143], v[56:59], v[8:11], v[128:143]
	v_exp_f32_e32 v112, v112
	v_exp_f32_e32 v113, v113
	v_exp_f32_e32 v114, v114
	v_exp_f32_e32 v115, v115
	v_pk_add_f32 v[160:161], v[160:161], v[108:109]
	v_pk_add_f32 v[162:163], v[162:163], v[110:111]
	v_mfma_f32_32x32x16_f16 v[144:159], v[56:59], v[24:27], v[144:159]
	v_exp_f32_e32 v116, v116
	v_exp_f32_e32 v117, v117
	v_exp_f32_e32 v118, v118
	v_exp_f32_e32 v119, v119
	v_pk_add_f32 v[164:165], v[164:165], v[112:113]
	v_pk_add_f32 v[166:167], v[166:167], v[114:115]
	v_mfma_f32_32x32x16_f16 v[128:143], v[60:63], v[12:15], v[128:143]
	v_exp_f32_e32 v120, v120
	v_exp_f32_e32 v121, v121
	v_exp_f32_e32 v122, v122
	v_exp_f32_e32 v123, v123
	v_pk_add_f32 v[164:165], v[164:165], v[116:117]
	v_pk_add_f32 v[166:167], v[166:167], v[118:119]
	v_mfma_f32_32x32x16_f16 v[144:159], v[60:63], v[28:31], v[144:159]
	v_exp_f32_e32 v124, v124
	v_exp_f32_e32 v125, v125
	v_exp_f32_e32 v126, v126
	v_exp_f32_e32 v127, v127
	v_pk_add_f32 v[164:165], v[164:165], v[120:121]
	v_pk_add_f32 v[166:167], v[166:167], v[122:123]
	s_nop 0
	v_pk_add_f32 v[164:165], v[164:165], v[124:125]
	v_pk_add_f32 v[166:167], v[166:167], v[126:127]
	global_load_dwordx4 v[48:51], v171, s[4:5] offset:0
	global_load_dwordx4 v[52:55], v171, s[4:5] offset:1024
	global_load_dwordx4 v[56:59], v171, s[4:5] offset:2048
	global_load_dwordx4 v[60:63], v171, s[4:5] offset:3072
	s_add_u32 s4, s4, 0x1000
	s_addc_u32 s5, s5, 0
	s_waitcnt vmcnt(12)
	v_mfma_f32_32x32x16_f16 v[96:111], v[64:67], v[0:3], 0
	v_exp_f32_e32 v128, v128
	v_exp_f32_e32 v129, v129
	v_exp_f32_e32 v130, v130
	v_exp_f32_e32 v131, v131
	v_mfma_f32_32x32x16_f16 v[112:127], v[64:67], v[16:19], 0
	v_exp_f32_e32 v132, v132
	v_exp_f32_e32 v133, v133
	v_exp_f32_e32 v134, v134
	v_exp_f32_e32 v135, v135
	v_pk_add_f32 v[160:161], v[160:161], v[128:129]
	v_pk_add_f32 v[162:163], v[162:163], v[130:131]
	v_mfma_f32_32x32x16_f16 v[96:111], v[68:71], v[4:7], v[96:111]
	v_exp_f32_e32 v136, v136
	v_exp_f32_e32 v137, v137
	v_exp_f32_e32 v138, v138
	v_exp_f32_e32 v139, v139
	v_pk_add_f32 v[160:161], v[160:161], v[132:133]
	v_pk_add_f32 v[162:163], v[162:163], v[134:135]
	v_mfma_f32_32x32x16_f16 v[112:127], v[68:71], v[20:23], v[112:127]
	v_exp_f32_e32 v140, v140
	v_exp_f32_e32 v141, v141
	v_exp_f32_e32 v142, v142
	v_exp_f32_e32 v143, v143
	v_pk_add_f32 v[160:161], v[160:161], v[136:137]
	v_pk_add_f32 v[162:163], v[162:163], v[138:139]
	v_mfma_f32_32x32x16_f16 v[96:111], v[72:75], v[8:11], v[96:111]
	v_exp_f32_e32 v144, v144
	v_exp_f32_e32 v145, v145
	v_exp_f32_e32 v146, v146
	v_exp_f32_e32 v147, v147
	v_pk_add_f32 v[160:161], v[160:161], v[140:141]
	v_pk_add_f32 v[162:163], v[162:163], v[142:143]
	v_mfma_f32_32x32x16_f16 v[112:127], v[72:75], v[24:27], v[112:127]
	v_exp_f32_e32 v148, v148
	v_exp_f32_e32 v149, v149
	v_exp_f32_e32 v150, v150
	v_exp_f32_e32 v151, v151
	v_pk_add_f32 v[164:165], v[164:165], v[144:145]
	v_pk_add_f32 v[166:167], v[166:167], v[146:147]
	v_mfma_f32_32x32x16_f16 v[96:111], v[76:79], v[12:15], v[96:111]
	v_exp_f32_e32 v152, v152
	v_exp_f32_e32 v153, v153
	v_exp_f32_e32 v154, v154
	v_exp_f32_e32 v155, v155
	v_pk_add_f32 v[164:165], v[164:165], v[148:149]
	v_pk_add_f32 v[166:167], v[166:167], v[150:151]
	v_mfma_f32_32x32x16_f16 v[112:127], v[76:79], v[28:31], v[112:127]
	v_exp_f32_e32 v156, v156
	v_exp_f32_e32 v157, v157
	v_exp_f32_e32 v158, v158
	v_exp_f32_e32 v159, v159
	v_pk_add_f32 v[164:165], v[164:165], v[152:153]
	v_pk_add_f32 v[166:167], v[166:167], v[154:155]
	s_nop 0
	v_pk_add_f32 v[164:165], v[164:165], v[156:157]
	v_pk_add_f32 v[166:167], v[166:167], v[158:159]
	global_load_dwordx4 v[64:67], v171, s[4:5] offset:0
	global_load_dwordx4 v[68:71], v171, s[4:5] offset:1024
	global_load_dwordx4 v[72:75], v171, s[4:5] offset:2048
	global_load_dwordx4 v[76:79], v171, s[4:5] offset:3072
	s_add_u32 s4, s4, 0x1000
	s_addc_u32 s5, s5, 0
	s_waitcnt vmcnt(12)
	v_mfma_f32_32x32x16_f16 v[128:143], v[80:83], v[0:3], 0
	v_exp_f32_e32 v96, v96
	v_exp_f32_e32 v97, v97
	v_exp_f32_e32 v98, v98
	v_exp_f32_e32 v99, v99
	v_mfma_f32_32x32x16_f16 v[144:159], v[80:83], v[16:19], 0
	v_exp_f32_e32 v100, v100
	v_exp_f32_e32 v101, v101
	v_exp_f32_e32 v102, v102
	v_exp_f32_e32 v103, v103
	v_pk_add_f32 v[160:161], v[160:161], v[96:97]
	v_pk_add_f32 v[162:163], v[162:163], v[98:99]
	v_mfma_f32_32x32x16_f16 v[128:143], v[84:87], v[4:7], v[128:143]
	v_exp_f32_e32 v104, v104
	v_exp_f32_e32 v105, v105
	v_exp_f32_e32 v106, v106
	v_exp_f32_e32 v107, v107
	v_pk_add_f32 v[160:161], v[160:161], v[100:101]
	v_pk_add_f32 v[162:163], v[162:163], v[102:103]
	v_mfma_f32_32x32x16_f16 v[144:159], v[84:87], v[20:23], v[144:159]
	v_exp_f32_e32 v108, v108
	v_exp_f32_e32 v109, v109
	v_exp_f32_e32 v110, v110
	v_exp_f32_e32 v111, v111
	v_pk_add_f32 v[160:161], v[160:161], v[104:105]
	v_pk_add_f32 v[162:163], v[162:163], v[106:107]
	v_mfma_f32_32x32x16_f16 v[128:143], v[88:91], v[8:11], v[128:143]
	v_exp_f32_e32 v112, v112
	v_exp_f32_e32 v113, v113
	v_exp_f32_e32 v114, v114
	v_exp_f32_e32 v115, v115
	v_pk_add_f32 v[160:161], v[160:161], v[108:109]
	v_pk_add_f32 v[162:163], v[162:163], v[110:111]
	v_mfma_f32_32x32x16_f16 v[144:159], v[88:91], v[24:27], v[144:159]
	v_exp_f32_e32 v116, v116
	v_exp_f32_e32 v117, v117
	v_exp_f32_e32 v118, v118
	v_exp_f32_e32 v119, v119
	v_pk_add_f32 v[164:165], v[164:165], v[112:113]
	v_pk_add_f32 v[166:167], v[166:167], v[114:115]
	v_mfma_f32_32x32x16_f16 v[128:143], v[92:95], v[12:15], v[128:143]
	v_exp_f32_e32 v120, v120
	v_exp_f32_e32 v121, v121
	v_exp_f32_e32 v122, v122
	v_exp_f32_e32 v123, v123
	v_pk_add_f32 v[164:165], v[164:165], v[116:117]
	v_pk_add_f32 v[166:167], v[166:167], v[118:119]
	v_mfma_f32_32x32x16_f16 v[144:159], v[92:95], v[28:31], v[144:159]
	v_exp_f32_e32 v124, v124
	v_exp_f32_e32 v125, v125
	v_exp_f32_e32 v126, v126
	v_exp_f32_e32 v127, v127
	v_pk_add_f32 v[164:165], v[164:165], v[120:121]
	v_pk_add_f32 v[166:167], v[166:167], v[122:123]
	s_nop 0
	v_pk_add_f32 v[164:165], v[164:165], v[124:125]
	v_pk_add_f32 v[166:167], v[166:167], v[126:127]
	global_load_dwordx4 v[80:83], v171, s[4:5] offset:0
	global_load_dwordx4 v[84:87], v171, s[4:5] offset:1024
	global_load_dwordx4 v[88:91], v171, s[4:5] offset:2048
	global_load_dwordx4 v[92:95], v171, s[4:5] offset:3072
	s_add_u32 s4, s4, 0x1000
	s_addc_u32 s5, s5, 0
	s_waitcnt vmcnt(12)
	v_mfma_f32_32x32x16_f16 v[96:111], v[32:35], v[0:3], 0
	v_exp_f32_e32 v128, v128
	v_exp_f32_e32 v129, v129
	v_exp_f32_e32 v130, v130
	v_exp_f32_e32 v131, v131
	v_mfma_f32_32x32x16_f16 v[112:127], v[32:35], v[16:19], 0
	v_exp_f32_e32 v132, v132
	v_exp_f32_e32 v133, v133
	v_exp_f32_e32 v134, v134
	v_exp_f32_e32 v135, v135
	v_pk_add_f32 v[160:161], v[160:161], v[128:129]
	v_pk_add_f32 v[162:163], v[162:163], v[130:131]
	v_mfma_f32_32x32x16_f16 v[96:111], v[36:39], v[4:7], v[96:111]
	v_exp_f32_e32 v136, v136
	v_exp_f32_e32 v137, v137
	v_exp_f32_e32 v138, v138
	v_exp_f32_e32 v139, v139
	v_pk_add_f32 v[160:161], v[160:161], v[132:133]
	v_pk_add_f32 v[162:163], v[162:163], v[134:135]
	v_mfma_f32_32x32x16_f16 v[112:127], v[36:39], v[20:23], v[112:127]
	v_exp_f32_e32 v140, v140
	v_exp_f32_e32 v141, v141
	v_exp_f32_e32 v142, v142
	v_exp_f32_e32 v143, v143
	v_pk_add_f32 v[160:161], v[160:161], v[136:137]
	v_pk_add_f32 v[162:163], v[162:163], v[138:139]
	v_mfma_f32_32x32x16_f16 v[96:111], v[40:43], v[8:11], v[96:111]
	v_exp_f32_e32 v144, v144
	v_exp_f32_e32 v145, v145
	v_exp_f32_e32 v146, v146
	v_exp_f32_e32 v147, v147
	v_pk_add_f32 v[160:161], v[160:161], v[140:141]
	v_pk_add_f32 v[162:163], v[162:163], v[142:143]
	v_mfma_f32_32x32x16_f16 v[112:127], v[40:43], v[24:27], v[112:127]
	v_exp_f32_e32 v148, v148
	v_exp_f32_e32 v149, v149
	v_exp_f32_e32 v150, v150
	v_exp_f32_e32 v151, v151
	v_pk_add_f32 v[164:165], v[164:165], v[144:145]
	v_pk_add_f32 v[166:167], v[166:167], v[146:147]
	v_mfma_f32_32x32x16_f16 v[96:111], v[44:47], v[12:15], v[96:111]
	v_exp_f32_e32 v152, v152
	v_exp_f32_e32 v153, v153
	v_exp_f32_e32 v154, v154
	v_exp_f32_e32 v155, v155
	v_pk_add_f32 v[164:165], v[164:165], v[148:149]
	v_pk_add_f32 v[166:167], v[166:167], v[150:151]
	v_mfma_f32_32x32x16_f16 v[112:127], v[44:47], v[28:31], v[112:127]
	v_exp_f32_e32 v156, v156
	v_exp_f32_e32 v157, v157
	v_exp_f32_e32 v158, v158
	v_exp_f32_e32 v159, v159
	v_pk_add_f32 v[164:165], v[164:165], v[152:153]
	v_pk_add_f32 v[166:167], v[166:167], v[154:155]
	s_nop 0
	v_pk_add_f32 v[164:165], v[164:165], v[156:157]
	v_pk_add_f32 v[166:167], v[166:167], v[158:159]
	global_load_dwordx4 v[32:35], v171, s[4:5] offset:0
	global_load_dwordx4 v[36:39], v171, s[4:5] offset:1024
	global_load_dwordx4 v[40:43], v171, s[4:5] offset:2048
	global_load_dwordx4 v[44:47], v171, s[4:5] offset:3072
	s_add_u32 s4, s4, 0x1000
	s_addc_u32 s5, s5, 0
	s_waitcnt vmcnt(12)
	v_mfma_f32_32x32x16_f16 v[128:143], v[48:51], v[0:3], 0
	v_exp_f32_e32 v96, v96
	v_exp_f32_e32 v97, v97
	v_exp_f32_e32 v98, v98
	v_exp_f32_e32 v99, v99
	v_mfma_f32_32x32x16_f16 v[144:159], v[48:51], v[16:19], 0
	v_exp_f32_e32 v100, v100
	v_exp_f32_e32 v101, v101
	v_exp_f32_e32 v102, v102
	v_exp_f32_e32 v103, v103
	v_pk_add_f32 v[160:161], v[160:161], v[96:97]
	v_pk_add_f32 v[162:163], v[162:163], v[98:99]
	v_mfma_f32_32x32x16_f16 v[128:143], v[52:55], v[4:7], v[128:143]
	v_exp_f32_e32 v104, v104
	v_exp_f32_e32 v105, v105
	v_exp_f32_e32 v106, v106
	v_exp_f32_e32 v107, v107
	v_pk_add_f32 v[160:161], v[160:161], v[100:101]
	v_pk_add_f32 v[162:163], v[162:163], v[102:103]
	v_mfma_f32_32x32x16_f16 v[144:159], v[52:55], v[20:23], v[144:159]
	v_exp_f32_e32 v108, v108
	v_exp_f32_e32 v109, v109
	v_exp_f32_e32 v110, v110
	v_exp_f32_e32 v111, v111
	v_pk_add_f32 v[160:161], v[160:161], v[104:105]
	v_pk_add_f32 v[162:163], v[162:163], v[106:107]
	v_mfma_f32_32x32x16_f16 v[128:143], v[56:59], v[8:11], v[128:143]
	v_exp_f32_e32 v112, v112
	v_exp_f32_e32 v113, v113
	v_exp_f32_e32 v114, v114
	v_exp_f32_e32 v115, v115
	v_pk_add_f32 v[160:161], v[160:161], v[108:109]
	v_pk_add_f32 v[162:163], v[162:163], v[110:111]
	v_mfma_f32_32x32x16_f16 v[144:159], v[56:59], v[24:27], v[144:159]
	v_exp_f32_e32 v116, v116
	v_exp_f32_e32 v117, v117
	v_exp_f32_e32 v118, v118
	v_exp_f32_e32 v119, v119
	v_pk_add_f32 v[164:165], v[164:165], v[112:113]
	v_pk_add_f32 v[166:167], v[166:167], v[114:115]
	v_mfma_f32_32x32x16_f16 v[128:143], v[60:63], v[12:15], v[128:143]
	v_exp_f32_e32 v120, v120
	v_exp_f32_e32 v121, v121
	v_exp_f32_e32 v122, v122
	v_exp_f32_e32 v123, v123
	v_pk_add_f32 v[164:165], v[164:165], v[116:117]
	v_pk_add_f32 v[166:167], v[166:167], v[118:119]
	v_mfma_f32_32x32x16_f16 v[144:159], v[60:63], v[28:31], v[144:159]
	v_exp_f32_e32 v124, v124
	v_exp_f32_e32 v125, v125
	v_exp_f32_e32 v126, v126
	v_exp_f32_e32 v127, v127
	v_pk_add_f32 v[164:165], v[164:165], v[120:121]
	v_pk_add_f32 v[166:167], v[166:167], v[122:123]
	s_nop 0
	v_pk_add_f32 v[164:165], v[164:165], v[124:125]
	v_pk_add_f32 v[166:167], v[166:167], v[126:127]
	global_load_dwordx4 v[48:51], v171, s[4:5] offset:0
	global_load_dwordx4 v[52:55], v171, s[4:5] offset:1024
	global_load_dwordx4 v[56:59], v171, s[4:5] offset:2048
	global_load_dwordx4 v[60:63], v171, s[4:5] offset:3072
	s_add_u32 s4, s4, 0x1000
	s_addc_u32 s5, s5, 0
	s_waitcnt vmcnt(12)
	v_mfma_f32_32x32x16_f16 v[96:111], v[64:67], v[0:3], 0
	v_exp_f32_e32 v128, v128
	v_exp_f32_e32 v129, v129
	v_exp_f32_e32 v130, v130
	v_exp_f32_e32 v131, v131
	v_mfma_f32_32x32x16_f16 v[112:127], v[64:67], v[16:19], 0
	v_exp_f32_e32 v132, v132
	v_exp_f32_e32 v133, v133
	v_exp_f32_e32 v134, v134
	v_exp_f32_e32 v135, v135
	v_pk_add_f32 v[160:161], v[160:161], v[128:129]
	v_pk_add_f32 v[162:163], v[162:163], v[130:131]
	v_mfma_f32_32x32x16_f16 v[96:111], v[68:71], v[4:7], v[96:111]
	v_exp_f32_e32 v136, v136
	v_exp_f32_e32 v137, v137
	v_exp_f32_e32 v138, v138
	v_exp_f32_e32 v139, v139
	v_pk_add_f32 v[160:161], v[160:161], v[132:133]
	v_pk_add_f32 v[162:163], v[162:163], v[134:135]
	v_mfma_f32_32x32x16_f16 v[112:127], v[68:71], v[20:23], v[112:127]
	v_exp_f32_e32 v140, v140
	v_exp_f32_e32 v141, v141
	v_exp_f32_e32 v142, v142
	v_exp_f32_e32 v143, v143
	v_pk_add_f32 v[160:161], v[160:161], v[136:137]
	v_pk_add_f32 v[162:163], v[162:163], v[138:139]
	v_mfma_f32_32x32x16_f16 v[96:111], v[72:75], v[8:11], v[96:111]
	v_exp_f32_e32 v144, v144
	v_exp_f32_e32 v145, v145
	v_exp_f32_e32 v146, v146
	v_exp_f32_e32 v147, v147
	v_pk_add_f32 v[160:161], v[160:161], v[140:141]
	v_pk_add_f32 v[162:163], v[162:163], v[142:143]
	v_mfma_f32_32x32x16_f16 v[112:127], v[72:75], v[24:27], v[112:127]
	v_exp_f32_e32 v148, v148
	v_exp_f32_e32 v149, v149
	v_exp_f32_e32 v150, v150
	v_exp_f32_e32 v151, v151
	v_pk_add_f32 v[164:165], v[164:165], v[144:145]
	v_pk_add_f32 v[166:167], v[166:167], v[146:147]
	v_mfma_f32_32x32x16_f16 v[96:111], v[76:79], v[12:15], v[96:111]
	v_exp_f32_e32 v152, v152
	v_exp_f32_e32 v153, v153
	v_exp_f32_e32 v154, v154
	v_exp_f32_e32 v155, v155
	v_pk_add_f32 v[164:165], v[164:165], v[148:149]
	v_pk_add_f32 v[166:167], v[166:167], v[150:151]
	v_mfma_f32_32x32x16_f16 v[112:127], v[76:79], v[28:31], v[112:127]
	v_exp_f32_e32 v156, v156
	v_exp_f32_e32 v157, v157
	v_exp_f32_e32 v158, v158
	v_exp_f32_e32 v159, v159
	v_pk_add_f32 v[164:165], v[164:165], v[152:153]
	v_pk_add_f32 v[166:167], v[166:167], v[154:155]
	s_nop 0
	v_pk_add_f32 v[164:165], v[164:165], v[156:157]
	v_pk_add_f32 v[166:167], v[166:167], v[158:159]
	global_load_dwordx4 v[64:67], v171, s[4:5] offset:0
	global_load_dwordx4 v[68:71], v171, s[4:5] offset:1024
	global_load_dwordx4 v[72:75], v171, s[4:5] offset:2048
	global_load_dwordx4 v[76:79], v171, s[4:5] offset:3072
	s_add_u32 s4, s4, 0x1000
	s_addc_u32 s5, s5, 0
	s_waitcnt vmcnt(12)
	v_mfma_f32_32x32x16_f16 v[128:143], v[80:83], v[0:3], 0
	v_exp_f32_e32 v96, v96
	v_exp_f32_e32 v97, v97
	v_exp_f32_e32 v98, v98
	v_exp_f32_e32 v99, v99
	v_mfma_f32_32x32x16_f16 v[144:159], v[80:83], v[16:19], 0
	v_exp_f32_e32 v100, v100
	v_exp_f32_e32 v101, v101
	v_exp_f32_e32 v102, v102
	v_exp_f32_e32 v103, v103
	v_pk_add_f32 v[160:161], v[160:161], v[96:97]
	v_pk_add_f32 v[162:163], v[162:163], v[98:99]
	v_mfma_f32_32x32x16_f16 v[128:143], v[84:87], v[4:7], v[128:143]
	v_exp_f32_e32 v104, v104
	v_exp_f32_e32 v105, v105
	v_exp_f32_e32 v106, v106
	v_exp_f32_e32 v107, v107
	v_pk_add_f32 v[160:161], v[160:161], v[100:101]
	v_pk_add_f32 v[162:163], v[162:163], v[102:103]
	v_mfma_f32_32x32x16_f16 v[144:159], v[84:87], v[20:23], v[144:159]
	v_exp_f32_e32 v108, v108
	v_exp_f32_e32 v109, v109
	v_exp_f32_e32 v110, v110
	v_exp_f32_e32 v111, v111
	v_pk_add_f32 v[160:161], v[160:161], v[104:105]
	v_pk_add_f32 v[162:163], v[162:163], v[106:107]
	v_mfma_f32_32x32x16_f16 v[128:143], v[88:91], v[8:11], v[128:143]
	v_exp_f32_e32 v112, v112
	v_exp_f32_e32 v113, v113
	v_exp_f32_e32 v114, v114
	v_exp_f32_e32 v115, v115
	v_pk_add_f32 v[160:161], v[160:161], v[108:109]
	v_pk_add_f32 v[162:163], v[162:163], v[110:111]
	v_mfma_f32_32x32x16_f16 v[144:159], v[88:91], v[24:27], v[144:159]
	v_exp_f32_e32 v116, v116
	v_exp_f32_e32 v117, v117
	v_exp_f32_e32 v118, v118
	v_exp_f32_e32 v119, v119
	v_pk_add_f32 v[164:165], v[164:165], v[112:113]
	v_pk_add_f32 v[166:167], v[166:167], v[114:115]
	v_mfma_f32_32x32x16_f16 v[128:143], v[92:95], v[12:15], v[128:143]
	v_exp_f32_e32 v120, v120
	v_exp_f32_e32 v121, v121
	v_exp_f32_e32 v122, v122
	v_exp_f32_e32 v123, v123
	v_pk_add_f32 v[164:165], v[164:165], v[116:117]
	v_pk_add_f32 v[166:167], v[166:167], v[118:119]
	v_mfma_f32_32x32x16_f16 v[144:159], v[92:95], v[28:31], v[144:159]
	v_exp_f32_e32 v124, v124
	v_exp_f32_e32 v125, v125
	v_exp_f32_e32 v126, v126
	v_exp_f32_e32 v127, v127
	v_pk_add_f32 v[164:165], v[164:165], v[120:121]
	v_pk_add_f32 v[166:167], v[166:167], v[122:123]
	s_nop 0
	v_pk_add_f32 v[164:165], v[164:165], v[124:125]
	v_pk_add_f32 v[166:167], v[166:167], v[126:127]
	global_load_dwordx4 v[80:83], v171, s[4:5] offset:0
	global_load_dwordx4 v[84:87], v171, s[4:5] offset:1024
	global_load_dwordx4 v[88:91], v171, s[4:5] offset:2048
	global_load_dwordx4 v[92:95], v171, s[4:5] offset:3072
	s_add_u32 s4, s4, 0x1000
	s_addc_u32 s5, s5, 0
	s_waitcnt vmcnt(12)
	v_mfma_f32_32x32x16_f16 v[96:111], v[32:35], v[0:3], 0
	v_exp_f32_e32 v128, v128
	v_exp_f32_e32 v129, v129
	v_exp_f32_e32 v130, v130
	v_exp_f32_e32 v131, v131
	v_mfma_f32_32x32x16_f16 v[112:127], v[32:35], v[16:19], 0
	v_exp_f32_e32 v132, v132
	v_exp_f32_e32 v133, v133
	v_exp_f32_e32 v134, v134
	v_exp_f32_e32 v135, v135
	v_pk_add_f32 v[160:161], v[160:161], v[128:129]
	v_pk_add_f32 v[162:163], v[162:163], v[130:131]
	v_mfma_f32_32x32x16_f16 v[96:111], v[36:39], v[4:7], v[96:111]
	v_exp_f32_e32 v136, v136
	v_exp_f32_e32 v137, v137
	v_exp_f32_e32 v138, v138
	v_exp_f32_e32 v139, v139
	v_pk_add_f32 v[160:161], v[160:161], v[132:133]
	v_pk_add_f32 v[162:163], v[162:163], v[134:135]
	v_mfma_f32_32x32x16_f16 v[112:127], v[36:39], v[20:23], v[112:127]
	v_exp_f32_e32 v140, v140
	v_exp_f32_e32 v141, v141
	v_exp_f32_e32 v142, v142
	v_exp_f32_e32 v143, v143
	v_pk_add_f32 v[160:161], v[160:161], v[136:137]
	v_pk_add_f32 v[162:163], v[162:163], v[138:139]
	v_mfma_f32_32x32x16_f16 v[96:111], v[40:43], v[8:11], v[96:111]
	v_exp_f32_e32 v144, v144
	v_exp_f32_e32 v145, v145
	v_exp_f32_e32 v146, v146
	v_exp_f32_e32 v147, v147
	v_pk_add_f32 v[160:161], v[160:161], v[140:141]
	v_pk_add_f32 v[162:163], v[162:163], v[142:143]
	v_mfma_f32_32x32x16_f16 v[112:127], v[40:43], v[24:27], v[112:127]
	v_exp_f32_e32 v148, v148
	v_exp_f32_e32 v149, v149
	v_exp_f32_e32 v150, v150
	v_exp_f32_e32 v151, v151
	v_pk_add_f32 v[164:165], v[164:165], v[144:145]
	v_pk_add_f32 v[166:167], v[166:167], v[146:147]
	v_mfma_f32_32x32x16_f16 v[96:111], v[44:47], v[12:15], v[96:111]
	v_exp_f32_e32 v152, v152
	v_exp_f32_e32 v153, v153
	v_exp_f32_e32 v154, v154
	v_exp_f32_e32 v155, v155
	v_pk_add_f32 v[164:165], v[164:165], v[148:149]
	v_pk_add_f32 v[166:167], v[166:167], v[150:151]
	v_mfma_f32_32x32x16_f16 v[112:127], v[44:47], v[28:31], v[112:127]
	v_exp_f32_e32 v156, v156
	v_exp_f32_e32 v157, v157
	v_exp_f32_e32 v158, v158
	v_exp_f32_e32 v159, v159
	v_pk_add_f32 v[164:165], v[164:165], v[152:153]
	v_pk_add_f32 v[166:167], v[166:167], v[154:155]
	s_nop 0
	v_pk_add_f32 v[164:165], v[164:165], v[156:157]
	v_pk_add_f32 v[166:167], v[166:167], v[158:159]
	s_waitcnt vmcnt(8)
	v_mfma_f32_32x32x16_f16 v[128:143], v[48:51], v[0:3], 0
	v_exp_f32_e32 v96, v96
	v_exp_f32_e32 v97, v97
	v_exp_f32_e32 v98, v98
	v_exp_f32_e32 v99, v99
	v_mfma_f32_32x32x16_f16 v[144:159], v[48:51], v[16:19], 0
	v_exp_f32_e32 v100, v100
	v_exp_f32_e32 v101, v101
	v_exp_f32_e32 v102, v102
	v_exp_f32_e32 v103, v103
	v_pk_add_f32 v[160:161], v[160:161], v[96:97]
	v_pk_add_f32 v[162:163], v[162:163], v[98:99]
	v_mfma_f32_32x32x16_f16 v[128:143], v[52:55], v[4:7], v[128:143]
	v_exp_f32_e32 v104, v104
	v_exp_f32_e32 v105, v105
	v_exp_f32_e32 v106, v106
	v_exp_f32_e32 v107, v107
	v_pk_add_f32 v[160:161], v[160:161], v[100:101]
	v_pk_add_f32 v[162:163], v[162:163], v[102:103]
	v_mfma_f32_32x32x16_f16 v[144:159], v[52:55], v[20:23], v[144:159]
	v_exp_f32_e32 v108, v108
	v_exp_f32_e32 v109, v109
	v_exp_f32_e32 v110, v110
	v_exp_f32_e32 v111, v111
	v_pk_add_f32 v[160:161], v[160:161], v[104:105]
	v_pk_add_f32 v[162:163], v[162:163], v[106:107]
	v_mfma_f32_32x32x16_f16 v[128:143], v[56:59], v[8:11], v[128:143]
	v_exp_f32_e32 v112, v112
	v_exp_f32_e32 v113, v113
	v_exp_f32_e32 v114, v114
	v_exp_f32_e32 v115, v115
	v_pk_add_f32 v[160:161], v[160:161], v[108:109]
	v_pk_add_f32 v[162:163], v[162:163], v[110:111]
	v_mfma_f32_32x32x16_f16 v[144:159], v[56:59], v[24:27], v[144:159]
	v_exp_f32_e32 v116, v116
	v_exp_f32_e32 v117, v117
	v_exp_f32_e32 v118, v118
	v_exp_f32_e32 v119, v119
	v_pk_add_f32 v[164:165], v[164:165], v[112:113]
	v_pk_add_f32 v[166:167], v[166:167], v[114:115]
	v_mfma_f32_32x32x16_f16 v[128:143], v[60:63], v[12:15], v[128:143]
	v_exp_f32_e32 v120, v120
	v_exp_f32_e32 v121, v121
	v_exp_f32_e32 v122, v122
	v_exp_f32_e32 v123, v123
	v_pk_add_f32 v[164:165], v[164:165], v[116:117]
	v_pk_add_f32 v[166:167], v[166:167], v[118:119]
	v_mfma_f32_32x32x16_f16 v[144:159], v[60:63], v[28:31], v[144:159]
	v_exp_f32_e32 v124, v124
	v_exp_f32_e32 v125, v125
	v_exp_f32_e32 v126, v126
	v_exp_f32_e32 v127, v127
	v_pk_add_f32 v[164:165], v[164:165], v[120:121]
	v_pk_add_f32 v[166:167], v[166:167], v[122:123]
	s_nop 0
	v_pk_add_f32 v[164:165], v[164:165], v[124:125]
	v_pk_add_f32 v[166:167], v[166:167], v[126:127]
	s_waitcnt vmcnt(4)
	v_mfma_f32_32x32x16_f16 v[96:111], v[64:67], v[0:3], 0
	v_exp_f32_e32 v128, v128
	v_exp_f32_e32 v129, v129
	v_exp_f32_e32 v130, v130
	v_exp_f32_e32 v131, v131
	v_mfma_f32_32x32x16_f16 v[112:127], v[64:67], v[16:19], 0
	v_exp_f32_e32 v132, v132
	v_exp_f32_e32 v133, v133
	v_exp_f32_e32 v134, v134
	v_exp_f32_e32 v135, v135
	v_pk_add_f32 v[160:161], v[160:161], v[128:129]
	v_pk_add_f32 v[162:163], v[162:163], v[130:131]
	v_mfma_f32_32x32x16_f16 v[96:111], v[68:71], v[4:7], v[96:111]
	v_exp_f32_e32 v136, v136
	v_exp_f32_e32 v137, v137
	v_exp_f32_e32 v138, v138
	v_exp_f32_e32 v139, v139
	v_pk_add_f32 v[160:161], v[160:161], v[132:133]
	v_pk_add_f32 v[162:163], v[162:163], v[134:135]
	v_mfma_f32_32x32x16_f16 v[112:127], v[68:71], v[20:23], v[112:127]
	v_exp_f32_e32 v140, v140
	v_exp_f32_e32 v141, v141
	v_exp_f32_e32 v142, v142
	v_exp_f32_e32 v143, v143
	v_pk_add_f32 v[160:161], v[160:161], v[136:137]
	v_pk_add_f32 v[162:163], v[162:163], v[138:139]
	v_mfma_f32_32x32x16_f16 v[96:111], v[72:75], v[8:11], v[96:111]
	v_exp_f32_e32 v144, v144
	v_exp_f32_e32 v145, v145
	v_exp_f32_e32 v146, v146
	v_exp_f32_e32 v147, v147
	v_pk_add_f32 v[160:161], v[160:161], v[140:141]
	v_pk_add_f32 v[162:163], v[162:163], v[142:143]
	v_mfma_f32_32x32x16_f16 v[112:127], v[72:75], v[24:27], v[112:127]
	v_exp_f32_e32 v148, v148
	v_exp_f32_e32 v149, v149
	v_exp_f32_e32 v150, v150
	v_exp_f32_e32 v151, v151
	v_pk_add_f32 v[164:165], v[164:165], v[144:145]
	v_pk_add_f32 v[166:167], v[166:167], v[146:147]
	v_mfma_f32_32x32x16_f16 v[96:111], v[76:79], v[12:15], v[96:111]
	v_exp_f32_e32 v152, v152
	v_exp_f32_e32 v153, v153
	v_exp_f32_e32 v154, v154
	v_exp_f32_e32 v155, v155
	v_pk_add_f32 v[164:165], v[164:165], v[148:149]
	v_pk_add_f32 v[166:167], v[166:167], v[150:151]
	v_mfma_f32_32x32x16_f16 v[112:127], v[76:79], v[28:31], v[112:127]
	v_exp_f32_e32 v156, v156
	v_exp_f32_e32 v157, v157
	v_exp_f32_e32 v158, v158
	v_exp_f32_e32 v159, v159
	v_pk_add_f32 v[164:165], v[164:165], v[152:153]
	v_pk_add_f32 v[166:167], v[166:167], v[154:155]
	s_nop 0
	v_pk_add_f32 v[164:165], v[164:165], v[156:157]
	v_pk_add_f32 v[166:167], v[166:167], v[158:159]
	s_waitcnt vmcnt(0)
	v_mfma_f32_32x32x16_f16 v[128:143], v[80:83], v[0:3], 0
	v_exp_f32_e32 v96, v96
	v_exp_f32_e32 v97, v97
	v_exp_f32_e32 v98, v98
	v_exp_f32_e32 v99, v99
	v_mfma_f32_32x32x16_f16 v[144:159], v[80:83], v[16:19], 0
	v_exp_f32_e32 v100, v100
	v_exp_f32_e32 v101, v101
	v_exp_f32_e32 v102, v102
	v_exp_f32_e32 v103, v103
	v_pk_add_f32 v[160:161], v[160:161], v[96:97]
	v_pk_add_f32 v[162:163], v[162:163], v[98:99]
	v_mfma_f32_32x32x16_f16 v[128:143], v[84:87], v[4:7], v[128:143]
	v_exp_f32_e32 v104, v104
	v_exp_f32_e32 v105, v105
	v_exp_f32_e32 v106, v106
	v_exp_f32_e32 v107, v107
	v_pk_add_f32 v[160:161], v[160:161], v[100:101]
	v_pk_add_f32 v[162:163], v[162:163], v[102:103]
	v_mfma_f32_32x32x16_f16 v[144:159], v[84:87], v[20:23], v[144:159]
	v_exp_f32_e32 v108, v108
	v_exp_f32_e32 v109, v109
	v_exp_f32_e32 v110, v110
	v_exp_f32_e32 v111, v111
	v_pk_add_f32 v[160:161], v[160:161], v[104:105]
	v_pk_add_f32 v[162:163], v[162:163], v[106:107]
	v_mfma_f32_32x32x16_f16 v[128:143], v[88:91], v[8:11], v[128:143]
	v_exp_f32_e32 v112, v112
	v_exp_f32_e32 v113, v113
	v_exp_f32_e32 v114, v114
	v_exp_f32_e32 v115, v115
	v_pk_add_f32 v[160:161], v[160:161], v[108:109]
	v_pk_add_f32 v[162:163], v[162:163], v[110:111]
	v_mfma_f32_32x32x16_f16 v[144:159], v[88:91], v[24:27], v[144:159]
	v_exp_f32_e32 v116, v116
	v_exp_f32_e32 v117, v117
	v_exp_f32_e32 v118, v118
	v_exp_f32_e32 v119, v119
	v_pk_add_f32 v[164:165], v[164:165], v[112:113]
	v_pk_add_f32 v[166:167], v[166:167], v[114:115]
	v_mfma_f32_32x32x16_f16 v[128:143], v[92:95], v[12:15], v[128:143]
	v_exp_f32_e32 v120, v120
	v_exp_f32_e32 v121, v121
	v_exp_f32_e32 v122, v122
	v_exp_f32_e32 v123, v123
	v_pk_add_f32 v[164:165], v[164:165], v[116:117]
	v_pk_add_f32 v[166:167], v[166:167], v[118:119]
	v_mfma_f32_32x32x16_f16 v[144:159], v[92:95], v[28:31], v[144:159]
	v_exp_f32_e32 v124, v124
	v_exp_f32_e32 v125, v125
	v_exp_f32_e32 v126, v126
	v_exp_f32_e32 v127, v127
	v_pk_add_f32 v[164:165], v[164:165], v[120:121]
	v_pk_add_f32 v[166:167], v[166:167], v[122:123]
	s_nop 0
	v_pk_add_f32 v[164:165], v[164:165], v[124:125]
	v_pk_add_f32 v[166:167], v[166:167], v[126:127]
	v_exp_f32_e32 v128, v128
	v_exp_f32_e32 v129, v129
	v_exp_f32_e32 v130, v130
	v_exp_f32_e32 v131, v131
	v_exp_f32_e32 v132, v132
	v_exp_f32_e32 v133, v133
	v_exp_f32_e32 v134, v134
	v_exp_f32_e32 v135, v135
	v_pk_add_f32 v[160:161], v[160:161], v[128:129]
	v_pk_add_f32 v[162:163], v[162:163], v[130:131]
	v_exp_f32_e32 v136, v136
	v_exp_f32_e32 v137, v137
	v_exp_f32_e32 v138, v138
	v_exp_f32_e32 v139, v139
	v_pk_add_f32 v[160:161], v[160:161], v[132:133]
	v_pk_add_f32 v[162:163], v[162:163], v[134:135]
	v_exp_f32_e32 v140, v140
	v_exp_f32_e32 v141, v141
	v_exp_f32_e32 v142, v142
	v_exp_f32_e32 v143, v143
	v_pk_add_f32 v[160:161], v[160:161], v[136:137]
	v_pk_add_f32 v[162:163], v[162:163], v[138:139]
	v_exp_f32_e32 v144, v144
	v_exp_f32_e32 v145, v145
	v_exp_f32_e32 v146, v146
	v_exp_f32_e32 v147, v147
	v_pk_add_f32 v[160:161], v[160:161], v[140:141]
	v_pk_add_f32 v[162:163], v[162:163], v[142:143]
	v_exp_f32_e32 v148, v148
	v_exp_f32_e32 v149, v149
	v_exp_f32_e32 v150, v150
	v_exp_f32_e32 v151, v151
	v_pk_add_f32 v[164:165], v[164:165], v[144:145]
	v_pk_add_f32 v[166:167], v[166:167], v[146:147]
	v_exp_f32_e32 v152, v152
	v_exp_f32_e32 v153, v153
	v_exp_f32_e32 v154, v154
	v_exp_f32_e32 v155, v155
	v_pk_add_f32 v[164:165], v[164:165], v[148:149]
	v_pk_add_f32 v[166:167], v[166:167], v[150:151]
	v_exp_f32_e32 v156, v156
	v_exp_f32_e32 v157, v157
	v_exp_f32_e32 v158, v158
	v_exp_f32_e32 v159, v159
	v_pk_add_f32 v[164:165], v[164:165], v[152:153]
	v_pk_add_f32 v[166:167], v[166:167], v[154:155]
	s_nop 0
	v_pk_add_f32 v[164:165], v[164:165], v[156:157]
	v_pk_add_f32 v[166:167], v[166:167], v[158:159]
	v_add_f32_e32 v160, v160, v161
	v_add_f32_e32 v162, v162, v163
	v_add_f32_e32 v164, v164, v165
	v_add_f32_e32 v166, v166, v167
	v_add_f32_e32 v160, v160, v162
	v_add_f32_e32 v164, v164, v166
	v_lshrrev_b32_e32 v168, 5, v172
	v_and_b32_e32 v169, 31, v172
	v_lshlrev_b32_e32 v168, 8, v168
	v_lshl_add_u32 v168, v173, 9, v168
	v_lshl_add_u32 v168, v169, 2, v168
	ds_write2_b32 v168, v160, v164 offset1:32
	s_waitcnt lgkmcnt(0)
	s_barrier
	s_cmp_lg_u32 s14, 0
	s_cbranch_scc1 .Lk2_done
	v_lshlrev_b32_e32 v168, 2, v170
	ds_read_b32 v0, v168 offset:0
	ds_read_b32 v1, v168 offset:256
	ds_read_b32 v2, v168 offset:512
	ds_read_b32 v3, v168 offset:768
	ds_read_b32 v4, v168 offset:1024
	ds_read_b32 v5, v168 offset:1280
	ds_read_b32 v6, v168 offset:1536
	ds_read_b32 v7, v168 offset:1792
	ds_read_b32 v8, v168 offset:2048
	ds_read_b32 v9, v168 offset:2304
	ds_read_b32 v10, v168 offset:2560
	ds_read_b32 v11, v168 offset:2816
	ds_read_b32 v12, v168 offset:3072
	ds_read_b32 v13, v168 offset:3328
	ds_read_b32 v14, v168 offset:3584
	ds_read_b32 v15, v168 offset:3840
	s_waitcnt lgkmcnt(0)
	v_add_f32_e32 v0, v0, v1
	v_add_f32_e32 v0, v0, v2
	v_add_f32_e32 v0, v0, v3
	v_add_f32_e32 v0, v0, v4
	v_add_f32_e32 v0, v0, v5
	v_add_f32_e32 v0, v0, v6
	v_add_f32_e32 v0, v0, v7
	v_add_f32_e32 v0, v0, v8
	v_add_f32_e32 v0, v0, v9
	v_add_f32_e32 v0, v0, v10
	v_add_f32_e32 v0, v0, v11
	v_add_f32_e32 v0, v0, v12
	v_add_f32_e32 v0, v0, v13
	v_add_f32_e32 v0, v0, v14
	v_add_f32_e32 v0, v0, v15
	v_log_f32_e32 v0, v0
	s_lshl_b32 s10, s10, 12
	s_lshl_b32 s11, s11, 5
	s_add_u32 s10, s10, s11
	v_add_u32_e32 v1, s10, v170
	v_lshlrev_b32_e32 v1, 2, v1
	v_sub_f32_e32 v0, 0x41400000, v0
	global_store_dword v1, v0, s[8:9]
